# v21 + fp6 K-loops: operand records in contiguous 8-register tuples, no v_mov / VALU-MFMA pads in the MFMA stream
# baseline (speedup 1.0000x reference)
.LBB0_1257:
	ds_read_b128 v[2:5], v202
	ds_read_b128 v[6:9], v202 offset:1024
	ds_read_b128 v[10:13], v202 offset:2048
	ds_read_b128 v[14:17], v202 offset:3072
	ds_read_b128 v[18:21], v203
	ds_read_b128 v[22:25], v203 offset:1024
	ds_read_b128 v[154:157], v203 offset:2048
	ds_read_b128 v[158:161], v203 offset:3072
	s_add_u32 s22, s20, 0xfffc0080
	s_addc_u32 s23, s21, -1
	s_cmp_eq_u32 s63, 12
	s_cselect_b32 s25, s11, s23
	s_cselect_b32 s24, s49, s22
	s_cselect_b32 s23, s13, s62
	s_cselect_b32 s22, s60, s61
	s_add_i32 m0, s35, 0xc000
	ds_read_b128 v[206:209], v204
	ds_read_b128 v[210:213], v204 offset:1024
	ds_read_b128 v[214:217], v204 offset:2048
	ds_read_b128 v[218:221], v204 offset:3072
	ds_read_b128 v[222:225], v204 offset:4096
	ds_read_b128 v[226:229], v204 offset:5120
	ds_read_b128 v[230:233], v204 offset:6144
	ds_read_b128 v[234:237], v204 offset:7168
	global_load_lds_dwordx4 v180, s[20:21]
	s_add_i32 m0, s35, 0xe000
	s_nop 0
	global_load_lds_dwordx4 v182, s[20:21]
	s_waitcnt vmcnt(8)
	s_waitcnt lgkmcnt(0)
	s_barrier
	s_setprio 1
	s_waitcnt lgkmcnt(0)
	v_mfma_scale_f32_16x16x128_f8f6f4 v[150:153], v[2:7], v[206:211], v[150:153], v8, v212 op_sel_hi:[0,0,0] cbsz:2 blgp:2
	v_mfma_scale_f32_16x16x128_f8f6f4 v[138:141], v[10:15], v[206:211], v[138:141], v16, v212 op_sel_hi:[0,0,0] cbsz:2 blgp:2
	v_mfma_scale_f32_16x16x128_f8f6f4 v[134:137], v[2:7], v[214:219], v[134:137], v8, v220 op_sel_hi:[0,0,0] cbsz:2 blgp:2
	v_mfma_scale_f32_16x16x128_f8f6f4 v[122:125], v[10:15], v[214:219], v[122:125], v16, v220 op_sel_hi:[0,0,0] cbsz:2 blgp:2
	v_mfma_scale_f32_16x16x128_f8f6f4 v[118:121], v[2:7], v[222:227], v[118:121], v8, v228 op_sel_hi:[0,0,0] cbsz:2 blgp:2
	v_mfma_scale_f32_16x16x128_f8f6f4 v[106:109], v[10:15], v[222:227], v[106:109], v16, v228 op_sel_hi:[0,0,0] cbsz:2 blgp:2
	v_mfma_scale_f32_16x16x128_f8f6f4 v[102:105], v[2:7], v[230:235], v[102:105], v8, v236 op_sel_hi:[0,0,0] cbsz:2 blgp:2
	v_mfma_scale_f32_16x16x128_f8f6f4 v[90:93], v[10:15], v[230:235], v[90:93], v16, v236 op_sel_hi:[0,0,0] cbsz:2 blgp:2
	s_setprio 0
	s_setprio 1
	v_mfma_scale_f32_16x16x128_f8f6f4 v[146:149], v[18:23], v[206:211], v[146:149], v24, v212 op_sel_hi:[0,0,0] cbsz:2 blgp:2
	v_mfma_scale_f32_16x16x128_f8f6f4 v[142:145], v[154:159], v[206:211], v[142:145], v160, v212 op_sel_hi:[0,0,0] cbsz:2 blgp:2
	v_mfma_scale_f32_16x16x128_f8f6f4 v[130:133], v[18:23], v[214:219], v[130:133], v24, v220 op_sel_hi:[0,0,0] cbsz:2 blgp:2
	v_mfma_scale_f32_16x16x128_f8f6f4 v[126:129], v[154:159], v[214:219], v[126:129], v160, v220 op_sel_hi:[0,0,0] cbsz:2 blgp:2
	v_mfma_scale_f32_16x16x128_f8f6f4 v[114:117], v[18:23], v[222:227], v[114:117], v24, v228 op_sel_hi:[0,0,0] cbsz:2 blgp:2
	v_mfma_scale_f32_16x16x128_f8f6f4 v[110:113], v[154:159], v[222:227], v[110:113], v160, v228 op_sel_hi:[0,0,0] cbsz:2 blgp:2
	v_mfma_scale_f32_16x16x128_f8f6f4 v[98:101], v[18:23], v[230:235], v[98:101], v24, v236 op_sel_hi:[0,0,0] cbsz:2 blgp:2
	v_mfma_scale_f32_16x16x128_f8f6f4 v[94:97], v[154:159], v[230:235], v[94:97], v160, v236 op_sel_hi:[0,0,0] cbsz:2 blgp:2
	s_setprio 0
	s_barrier
	s_add_i32 s64, s42, s27
	v_lshl_add_u64 v[184:185], s[22:23], 0, v[172:173]
	s_mov_b32 m0, s64
	ds_read_b128 v[206:209], v204 offset:16384
	ds_read_b128 v[210:213], v204 offset:17408
	ds_read_b128 v[214:217], v204 offset:18432
	ds_read_b128 v[218:221], v204 offset:19456
	ds_read_b128 v[222:225], v204 offset:20480
	ds_read_b128 v[226:229], v204 offset:21504
	ds_read_b128 v[230:233], v204 offset:22528
	ds_read_b128 v[234:237], v204 offset:23552
	global_load_lds_dwordx4 v172, s[22:23]
	s_add_i32 m0, s64, 0x2000
	s_add_u32 s64, s22, 0x40000
	v_lshl_add_u64 v[186:187], s[22:23], 0, v[174:175]
	s_addc_u32 s65, s23, 0
	s_add_i32 s66, s43, s27
	global_load_lds_dwordx4 v174, s[22:23]
	s_mov_b32 m0, s66
	v_lshl_add_u64 v[188:189], s[24:25], 0, v[178:179]
	global_load_lds_dwordx4 v172, s[64:65]
	s_add_i32 m0, s66, 0x2000
	v_lshl_add_u64 v[190:191], s[24:25], 0, v[176:177]
	global_load_lds_dwordx4 v174, s[64:65]
	s_mov_b32 m0, s35
	s_nop 0
	global_load_lds_dwordx4 v178, s[24:25]
	s_mov_b32 m0, s36
	s_nop 0
	global_load_lds_dwordx4 v176, s[24:25]
	s_waitcnt vmcnt(8)
	s_waitcnt lgkmcnt(0)
	s_barrier
	s_setprio 1
	s_waitcnt lgkmcnt(0)
	v_mfma_scale_f32_16x16x128_f8f6f4 v[86:89], v[2:7], v[206:211], v[86:89], v8, v212 op_sel_hi:[0,0,0] cbsz:2 blgp:2
	v_mfma_scale_f32_16x16x128_f8f6f4 v[74:77], v[10:15], v[206:211], v[74:77], v16, v212 op_sel_hi:[0,0,0] cbsz:2 blgp:2
	v_mfma_scale_f32_16x16x128_f8f6f4 v[70:73], v[2:7], v[214:219], v[70:73], v8, v220 op_sel_hi:[0,0,0] cbsz:2 blgp:2
	v_mfma_scale_f32_16x16x128_f8f6f4 v[58:61], v[10:15], v[214:219], v[58:61], v16, v220 op_sel_hi:[0,0,0] cbsz:2 blgp:2
	v_mfma_scale_f32_16x16x128_f8f6f4 v[54:57], v[2:7], v[222:227], v[54:57], v8, v228 op_sel_hi:[0,0,0] cbsz:2 blgp:2
	v_mfma_scale_f32_16x16x128_f8f6f4 v[42:45], v[10:15], v[222:227], v[42:45], v16, v228 op_sel_hi:[0,0,0] cbsz:2 blgp:2
	v_mfma_scale_f32_16x16x128_f8f6f4 v[38:41], v[2:7], v[230:235], v[38:41], v8, v236 op_sel_hi:[0,0,0] cbsz:2 blgp:2
	v_mfma_scale_f32_16x16x128_f8f6f4 v[26:29], v[10:15], v[230:235], v[26:29], v16, v236 op_sel_hi:[0,0,0] cbsz:2 blgp:2
	s_setprio 0
	s_setprio 1
	v_mfma_scale_f32_16x16x128_f8f6f4 v[82:85], v[18:23], v[206:211], v[82:85], v24, v212 op_sel_hi:[0,0,0] cbsz:2 blgp:2
	v_mfma_scale_f32_16x16x128_f8f6f4 v[78:81], v[154:159], v[206:211], v[78:81], v160, v212 op_sel_hi:[0,0,0] cbsz:2 blgp:2
	v_mfma_scale_f32_16x16x128_f8f6f4 v[66:69], v[18:23], v[214:219], v[66:69], v24, v220 op_sel_hi:[0,0,0] cbsz:2 blgp:2
	v_mfma_scale_f32_16x16x128_f8f6f4 v[62:65], v[154:159], v[214:219], v[62:65], v160, v220 op_sel_hi:[0,0,0] cbsz:2 blgp:2
	v_mfma_scale_f32_16x16x128_f8f6f4 v[50:53], v[18:23], v[222:227], v[50:53], v24, v228 op_sel_hi:[0,0,0] cbsz:2 blgp:2
	v_mfma_scale_f32_16x16x128_f8f6f4 v[46:49], v[154:159], v[222:227], v[46:49], v160, v228 op_sel_hi:[0,0,0] cbsz:2 blgp:2
	v_mfma_scale_f32_16x16x128_f8f6f4 v[34:37], v[18:23], v[230:235], v[34:37], v24, v236 op_sel_hi:[0,0,0] cbsz:2 blgp:2
	v_mfma_scale_f32_16x16x128_f8f6f4 v[30:33], v[154:159], v[230:235], v[30:33], v160, v236 op_sel_hi:[0,0,0] cbsz:2 blgp:2
	s_setprio 0
	s_barrier
	s_add_i32 s64, 0, 0x18000
	s_add_i32 s65, 0, 0x1c000
	v_add_u32_e32 v166, s64, v198
	v_add_u32_e32 v167, s65, v198
	ds_read_b128 v[2:5], v166
	ds_read_b128 v[6:9], v166 offset:1024
	ds_read_b128 v[10:13], v166 offset:2048
	ds_read_b128 v[14:17], v166 offset:3072
	ds_read_b128 v[18:21], v167
	ds_read_b128 v[22:25], v167 offset:1024
	ds_read_b128 v[154:157], v167 offset:2048
	ds_read_b128 v[158:161], v167 offset:3072
	s_add_u32 s24, s24, 0x40000
	s_addc_u32 s25, s25, 0
	s_mov_b32 m0, s37
	ds_read_b128 v[206:209], v204 offset:32768
	ds_read_b128 v[210:213], v204 offset:33792
	ds_read_b128 v[214:217], v204 offset:34816
	ds_read_b128 v[218:221], v204 offset:35840
	ds_read_b128 v[222:225], v204 offset:36864
	ds_read_b128 v[226:229], v204 offset:37888
	ds_read_b128 v[230:233], v204 offset:38912
	ds_read_b128 v[234:237], v204 offset:39936
	global_load_lds_dwordx4 v178, s[24:25]
	s_mov_b32 m0, s38
	s_nop 0
	global_load_lds_dwordx4 v176, s[24:25]
	s_waitcnt vmcnt(8)
	s_waitcnt lgkmcnt(0)
	s_barrier
	s_setprio 1
	s_waitcnt lgkmcnt(0)
	v_mfma_scale_f32_16x16x128_f8f6f4 v[150:153], v[2:7], v[206:211], v[150:153], v8, v212 op_sel_hi:[0,0,0] cbsz:2 blgp:2
	v_mfma_scale_f32_16x16x128_f8f6f4 v[138:141], v[10:15], v[206:211], v[138:141], v16, v212 op_sel_hi:[0,0,0] cbsz:2 blgp:2
	v_mfma_scale_f32_16x16x128_f8f6f4 v[134:137], v[2:7], v[214:219], v[134:137], v8, v220 op_sel_hi:[0,0,0] cbsz:2 blgp:2
	v_mfma_scale_f32_16x16x128_f8f6f4 v[122:125], v[10:15], v[214:219], v[122:125], v16, v220 op_sel_hi:[0,0,0] cbsz:2 blgp:2
	v_mfma_scale_f32_16x16x128_f8f6f4 v[118:121], v[2:7], v[222:227], v[118:121], v8, v228 op_sel_hi:[0,0,0] cbsz:2 blgp:2
	v_mfma_scale_f32_16x16x128_f8f6f4 v[106:109], v[10:15], v[222:227], v[106:109], v16, v228 op_sel_hi:[0,0,0] cbsz:2 blgp:2
	v_mfma_scale_f32_16x16x128_f8f6f4 v[102:105], v[2:7], v[230:235], v[102:105], v8, v236 op_sel_hi:[0,0,0] cbsz:2 blgp:2
	v_mfma_scale_f32_16x16x128_f8f6f4 v[90:93], v[10:15], v[230:235], v[90:93], v16, v236 op_sel_hi:[0,0,0] cbsz:2 blgp:2
	s_setprio 0
	s_setprio 1
	v_mfma_scale_f32_16x16x128_f8f6f4 v[146:149], v[18:23], v[206:211], v[146:149], v24, v212 op_sel_hi:[0,0,0] cbsz:2 blgp:2
	v_mfma_scale_f32_16x16x128_f8f6f4 v[142:145], v[154:159], v[206:211], v[142:145], v160, v212 op_sel_hi:[0,0,0] cbsz:2 blgp:2
	v_mfma_scale_f32_16x16x128_f8f6f4 v[130:133], v[18:23], v[214:219], v[130:133], v24, v220 op_sel_hi:[0,0,0] cbsz:2 blgp:2
	v_mfma_scale_f32_16x16x128_f8f6f4 v[126:129], v[154:159], v[214:219], v[126:129], v160, v220 op_sel_hi:[0,0,0] cbsz:2 blgp:2
	v_mfma_scale_f32_16x16x128_f8f6f4 v[114:117], v[18:23], v[222:227], v[114:117], v24, v228 op_sel_hi:[0,0,0] cbsz:2 blgp:2
	v_mfma_scale_f32_16x16x128_f8f6f4 v[110:113], v[154:159], v[222:227], v[110:113], v160, v228 op_sel_hi:[0,0,0] cbsz:2 blgp:2
	v_mfma_scale_f32_16x16x128_f8f6f4 v[98:101], v[18:23], v[230:235], v[98:101], v24, v236 op_sel_hi:[0,0,0] cbsz:2 blgp:2
	v_mfma_scale_f32_16x16x128_f8f6f4 v[94:97], v[154:159], v[230:235], v[94:97], v160, v236 op_sel_hi:[0,0,0] cbsz:2 blgp:2
	s_setprio 0
	s_barrier
	s_add_i32 s24, s64, s27
	v_lshl_add_u64 v[164:165], v[184:185], 0, s[6:7]
	s_mov_b32 m0, s24
	ds_read_b128 v[206:209], v204 offset:49152
	ds_read_b128 v[210:213], v204 offset:50176
	ds_read_b128 v[214:217], v204 offset:51200
	ds_read_b128 v[218:221], v204 offset:52224
	ds_read_b128 v[222:225], v204 offset:53248
	ds_read_b128 v[226:229], v204 offset:54272
	ds_read_b128 v[230:233], v204 offset:55296
	ds_read_b128 v[234:237], v204 offset:56320
	global_load_lds_dwordx4 v[164:165], off
	s_add_i32 m0, s24, 0x2000
	s_add_u32 s22, s22, 0x40080
	v_lshl_add_u64 v[164:165], v[186:187], 0, s[6:7]
	s_addc_u32 s23, s23, 0
	s_add_i32 s24, s65, s27
	global_load_lds_dwordx4 v[164:165], off
	s_mov_b32 m0, s24
	s_nop 0
	global_load_lds_dwordx4 v172, s[22:23]
	s_add_i32 m0, s24, 0x2000
	s_nop 0
	global_load_lds_dwordx4 v174, s[22:23]
	v_lshl_add_u64 v[164:165], v[188:189], 0, s[6:7]
	s_mov_b32 m0, s39
	s_nop 0
	global_load_lds_dwordx4 v[164:165], off
	v_lshl_add_u64 v[164:165], v[190:191], 0, s[6:7]
	s_mov_b32 m0, s40
	s_nop 0
	global_load_lds_dwordx4 v[164:165], off
	s_waitcnt vmcnt(8)
	s_waitcnt lgkmcnt(0)
	s_barrier
	s_setprio 1
	s_waitcnt lgkmcnt(0)
	v_mfma_scale_f32_16x16x128_f8f6f4 v[86:89], v[2:7], v[206:211], v[86:89], v8, v212 op_sel_hi:[0,0,0] cbsz:2 blgp:2
	v_mfma_scale_f32_16x16x128_f8f6f4 v[74:77], v[10:15], v[206:211], v[74:77], v16, v212 op_sel_hi:[0,0,0] cbsz:2 blgp:2
	v_mfma_scale_f32_16x16x128_f8f6f4 v[70:73], v[2:7], v[214:219], v[70:73], v8, v220 op_sel_hi:[0,0,0] cbsz:2 blgp:2
	v_mfma_scale_f32_16x16x128_f8f6f4 v[58:61], v[10:15], v[214:219], v[58:61], v16, v220 op_sel_hi:[0,0,0] cbsz:2 blgp:2
	v_mfma_scale_f32_16x16x128_f8f6f4 v[54:57], v[2:7], v[222:227], v[54:57], v8, v228 op_sel_hi:[0,0,0] cbsz:2 blgp:2
	v_mfma_scale_f32_16x16x128_f8f6f4 v[42:45], v[10:15], v[222:227], v[42:45], v16, v228 op_sel_hi:[0,0,0] cbsz:2 blgp:2
	v_mfma_scale_f32_16x16x128_f8f6f4 v[38:41], v[2:7], v[230:235], v[38:41], v8, v236 op_sel_hi:[0,0,0] cbsz:2 blgp:2
	v_mfma_scale_f32_16x16x128_f8f6f4 v[26:29], v[10:15], v[230:235], v[26:29], v16, v236 op_sel_hi:[0,0,0] cbsz:2 blgp:2
	s_setprio 0
	s_setprio 1
	v_mfma_scale_f32_16x16x128_f8f6f4 v[82:85], v[18:23], v[206:211], v[82:85], v24, v212 op_sel_hi:[0,0,0] cbsz:2 blgp:2
	v_mfma_scale_f32_16x16x128_f8f6f4 v[78:81], v[154:159], v[206:211], v[78:81], v160, v212 op_sel_hi:[0,0,0] cbsz:2 blgp:2
	v_mfma_scale_f32_16x16x128_f8f6f4 v[66:69], v[18:23], v[214:219], v[66:69], v24, v220 op_sel_hi:[0,0,0] cbsz:2 blgp:2
	v_mfma_scale_f32_16x16x128_f8f6f4 v[62:65], v[154:159], v[214:219], v[62:65], v160, v220 op_sel_hi:[0,0,0] cbsz:2 blgp:2
	v_mfma_scale_f32_16x16x128_f8f6f4 v[50:53], v[18:23], v[222:227], v[50:53], v24, v228 op_sel_hi:[0,0,0] cbsz:2 blgp:2
	v_mfma_scale_f32_16x16x128_f8f6f4 v[46:49], v[154:159], v[222:227], v[46:49], v160, v228 op_sel_hi:[0,0,0] cbsz:2 blgp:2
	v_mfma_scale_f32_16x16x128_f8f6f4 v[34:37], v[18:23], v[230:235], v[34:37], v24, v236 op_sel_hi:[0,0,0] cbsz:2 blgp:2
	v_mfma_scale_f32_16x16x128_f8f6f4 v[30:33], v[154:159], v[230:235], v[30:33], v160, v236 op_sel_hi:[0,0,0] cbsz:2 blgp:2
	s_setprio 0
	s_barrier
	s_add_i32 s63, s63, 2
	s_add_u32 s20, s20, 0x100
	s_addc_u32 s21, s21, 0
	s_add_u32 s61, s61, 0x100
	s_addc_u32 s62, s62, 0
	s_cmp_gt_u32 s63, 13
	s_cbranch_scc0 .LBB0_1257
	s_and_b64 vcc, exec, s[8:9]
	s_cbranch_vccz .LBB0_1260
	s_barrier

.LBB0_1279:
	ds_read_b128 v[2:5], v195
	ds_read_b128 v[6:9], v195 offset:1024
	ds_read_b128 v[10:13], v195 offset:2048
	ds_read_b128 v[14:17], v195 offset:3072
	ds_read_b128 v[18:21], v196
	ds_read_b128 v[22:25], v196 offset:1024
	ds_read_b128 v[154:157], v196 offset:2048
	ds_read_b128 v[158:161], v196 offset:3072
	s_add_u32 s24, s22, 0xfffc0080
	s_addc_u32 s25, s23, -1
	s_cmp_eq_u32 s61, 12
	s_cselect_b32 s27, s11, s25
	s_cselect_b32 s26, s49, s24
	s_cselect_b32 s25, s13, s60
	s_cselect_b32 s24, s50, s51
	s_mov_b32 m0, s46
	ds_read_b128 v[206:209], v198
	ds_read_b128 v[210:213], v198 offset:1024
	ds_read_b128 v[214:217], v198 offset:2048
	ds_read_b128 v[218:221], v198 offset:3072
	ds_read_b128 v[222:225], v198 offset:4096
	ds_read_b128 v[226:229], v198 offset:5120
	ds_read_b128 v[230:233], v198 offset:6144
	ds_read_b128 v[234:237], v198 offset:7168
	global_load_lds_dwordx4 v180, s[22:23]
	s_add_i32 m0, s21, 0xe000
	s_nop 0
	global_load_lds_dwordx4 v182, s[22:23]
	s_waitcnt vmcnt(8)
	s_waitcnt lgkmcnt(0)
	s_barrier
	s_setprio 1
	s_waitcnt lgkmcnt(0)
	v_mfma_scale_f32_16x16x128_f8f6f4 v[150:153], v[2:7], v[206:211], v[150:153], v8, v212 op_sel_hi:[0,0,0] cbsz:2 blgp:2
	v_mfma_scale_f32_16x16x128_f8f6f4 v[138:141], v[10:15], v[206:211], v[138:141], v16, v212 op_sel_hi:[0,0,0] cbsz:2 blgp:2
	v_mfma_scale_f32_16x16x128_f8f6f4 v[134:137], v[2:7], v[214:219], v[134:137], v8, v220 op_sel_hi:[0,0,0] cbsz:2 blgp:2
	v_mfma_scale_f32_16x16x128_f8f6f4 v[122:125], v[10:15], v[214:219], v[122:125], v16, v220 op_sel_hi:[0,0,0] cbsz:2 blgp:2
	v_mfma_scale_f32_16x16x128_f8f6f4 v[118:121], v[2:7], v[222:227], v[118:121], v8, v228 op_sel_hi:[0,0,0] cbsz:2 blgp:2
	v_mfma_scale_f32_16x16x128_f8f6f4 v[106:109], v[10:15], v[222:227], v[106:109], v16, v228 op_sel_hi:[0,0,0] cbsz:2 blgp:2
	v_mfma_scale_f32_16x16x128_f8f6f4 v[102:105], v[2:7], v[230:235], v[102:105], v8, v236 op_sel_hi:[0,0,0] cbsz:2 blgp:2
	v_mfma_scale_f32_16x16x128_f8f6f4 v[90:93], v[10:15], v[230:235], v[90:93], v16, v236 op_sel_hi:[0,0,0] cbsz:2 blgp:2
	s_setprio 0
	s_setprio 1
	v_mfma_scale_f32_16x16x128_f8f6f4 v[146:149], v[18:23], v[206:211], v[146:149], v24, v212 op_sel_hi:[0,0,0] cbsz:2 blgp:2
	v_mfma_scale_f32_16x16x128_f8f6f4 v[142:145], v[154:159], v[206:211], v[142:145], v160, v212 op_sel_hi:[0,0,0] cbsz:2 blgp:2
	v_mfma_scale_f32_16x16x128_f8f6f4 v[130:133], v[18:23], v[214:219], v[130:133], v24, v220 op_sel_hi:[0,0,0] cbsz:2 blgp:2
	v_mfma_scale_f32_16x16x128_f8f6f4 v[126:129], v[154:159], v[214:219], v[126:129], v160, v220 op_sel_hi:[0,0,0] cbsz:2 blgp:2
	v_mfma_scale_f32_16x16x128_f8f6f4 v[114:117], v[18:23], v[222:227], v[114:117], v24, v228 op_sel_hi:[0,0,0] cbsz:2 blgp:2
	v_mfma_scale_f32_16x16x128_f8f6f4 v[110:113], v[154:159], v[222:227], v[110:113], v160, v228 op_sel_hi:[0,0,0] cbsz:2 blgp:2
	v_mfma_scale_f32_16x16x128_f8f6f4 v[98:101], v[18:23], v[230:235], v[98:101], v24, v236 op_sel_hi:[0,0,0] cbsz:2 blgp:2
	v_mfma_scale_f32_16x16x128_f8f6f4 v[94:97], v[154:159], v[230:235], v[94:97], v160, v236 op_sel_hi:[0,0,0] cbsz:2 blgp:2
	s_setprio 0
	s_barrier
	s_add_i32 s62, s42, s35
	v_lshl_add_u64 v[184:185], s[24:25], 0, v[176:177]
	s_mov_b32 m0, s62
	ds_read_b128 v[206:209], v198 offset:16384
	ds_read_b128 v[210:213], v198 offset:17408
	ds_read_b128 v[214:217], v198 offset:18432
	ds_read_b128 v[218:221], v198 offset:19456
	ds_read_b128 v[222:225], v198 offset:20480
	ds_read_b128 v[226:229], v198 offset:21504
	ds_read_b128 v[230:233], v198 offset:22528
	ds_read_b128 v[234:237], v198 offset:23552
	global_load_lds_dwordx4 v176, s[24:25]
	s_add_i32 m0, s62, 0x2000
	s_add_u32 s62, s24, 0x40000
	v_lshl_add_u64 v[186:187], s[24:25], 0, v[172:173]
	s_addc_u32 s63, s25, 0
	s_add_i32 s64, s43, s35
	global_load_lds_dwordx4 v172, s[24:25]
	s_mov_b32 m0, s64
	v_lshl_add_u64 v[188:189], s[26:27], 0, v[178:179]
	global_load_lds_dwordx4 v176, s[62:63]
	s_add_i32 m0, s64, 0x2000
	v_lshl_add_u64 v[190:191], s[26:27], 0, v[174:175]
	global_load_lds_dwordx4 v172, s[62:63]
	s_mov_b32 m0, s21
	s_nop 0
	global_load_lds_dwordx4 v178, s[26:27]
	s_mov_b32 m0, s36
	s_nop 0
	global_load_lds_dwordx4 v174, s[26:27]
	s_waitcnt vmcnt(8)
	s_waitcnt lgkmcnt(0)
	s_barrier
	s_setprio 1
	s_waitcnt lgkmcnt(0)
	v_mfma_scale_f32_16x16x128_f8f6f4 v[86:89], v[2:7], v[206:211], v[86:89], v8, v212 op_sel_hi:[0,0,0] cbsz:2 blgp:2
	v_mfma_scale_f32_16x16x128_f8f6f4 v[74:77], v[10:15], v[206:211], v[74:77], v16, v212 op_sel_hi:[0,0,0] cbsz:2 blgp:2
	v_mfma_scale_f32_16x16x128_f8f6f4 v[70:73], v[2:7], v[214:219], v[70:73], v8, v220 op_sel_hi:[0,0,0] cbsz:2 blgp:2
	v_mfma_scale_f32_16x16x128_f8f6f4 v[58:61], v[10:15], v[214:219], v[58:61], v16, v220 op_sel_hi:[0,0,0] cbsz:2 blgp:2
	v_mfma_scale_f32_16x16x128_f8f6f4 v[54:57], v[2:7], v[222:227], v[54:57], v8, v228 op_sel_hi:[0,0,0] cbsz:2 blgp:2
	v_mfma_scale_f32_16x16x128_f8f6f4 v[42:45], v[10:15], v[222:227], v[42:45], v16, v228 op_sel_hi:[0,0,0] cbsz:2 blgp:2
	v_mfma_scale_f32_16x16x128_f8f6f4 v[38:41], v[2:7], v[230:235], v[38:41], v8, v236 op_sel_hi:[0,0,0] cbsz:2 blgp:2
	v_mfma_scale_f32_16x16x128_f8f6f4 v[26:29], v[10:15], v[230:235], v[26:29], v16, v236 op_sel_hi:[0,0,0] cbsz:2 blgp:2
	s_setprio 0
	s_setprio 1
	v_mfma_scale_f32_16x16x128_f8f6f4 v[82:85], v[18:23], v[206:211], v[82:85], v24, v212 op_sel_hi:[0,0,0] cbsz:2 blgp:2
	v_mfma_scale_f32_16x16x128_f8f6f4 v[78:81], v[154:159], v[206:211], v[78:81], v160, v212 op_sel_hi:[0,0,0] cbsz:2 blgp:2
	v_mfma_scale_f32_16x16x128_f8f6f4 v[66:69], v[18:23], v[214:219], v[66:69], v24, v220 op_sel_hi:[0,0,0] cbsz:2 blgp:2
	v_mfma_scale_f32_16x16x128_f8f6f4 v[62:65], v[154:159], v[214:219], v[62:65], v160, v220 op_sel_hi:[0,0,0] cbsz:2 blgp:2
	v_mfma_scale_f32_16x16x128_f8f6f4 v[50:53], v[18:23], v[222:227], v[50:53], v24, v228 op_sel_hi:[0,0,0] cbsz:2 blgp:2
	v_mfma_scale_f32_16x16x128_f8f6f4 v[46:49], v[154:159], v[222:227], v[46:49], v160, v228 op_sel_hi:[0,0,0] cbsz:2 blgp:2
	v_mfma_scale_f32_16x16x128_f8f6f4 v[34:37], v[18:23], v[230:235], v[34:37], v24, v236 op_sel_hi:[0,0,0] cbsz:2 blgp:2
	v_mfma_scale_f32_16x16x128_f8f6f4 v[30:33], v[154:159], v[230:235], v[30:33], v160, v236 op_sel_hi:[0,0,0] cbsz:2 blgp:2
	s_setprio 0
	s_barrier
	s_add_i32 s62, 0, 0x18000
	s_add_i32 s63, 0, 0x1c000
	v_add_u32_e32 v2, s62, v194
	v_add_u32_e32 v6, s63, v194
	ds_read_b128 v[2:5], v166
	ds_read_b128 v[6:9], v166 offset:1024
	ds_read_b128 v[10:13], v166 offset:2048
	ds_read_b128 v[14:17], v166 offset:3072
	ds_read_b128 v[18:21], v167
	ds_read_b128 v[22:25], v167 offset:1024
	ds_read_b128 v[154:157], v167 offset:2048
	ds_read_b128 v[158:161], v167 offset:3072
	s_add_u32 s26, s26, 0x40000
	s_addc_u32 s27, s27, 0
	s_mov_b32 m0, s37
	ds_read_b128 v[206:209], v198 offset:32768
	ds_read_b128 v[210:213], v198 offset:33792
	ds_read_b128 v[214:217], v198 offset:34816
	ds_read_b128 v[218:221], v198 offset:35840
	ds_read_b128 v[222:225], v198 offset:36864
	ds_read_b128 v[226:229], v198 offset:37888
	ds_read_b128 v[230:233], v198 offset:38912
	ds_read_b128 v[234:237], v198 offset:39936
	global_load_lds_dwordx4 v178, s[26:27]
	s_mov_b32 m0, s38
	s_nop 0
	global_load_lds_dwordx4 v174, s[26:27]
	s_waitcnt vmcnt(8)
	s_waitcnt lgkmcnt(0)
	s_barrier
	s_setprio 1
	s_waitcnt lgkmcnt(0)
	v_mfma_scale_f32_16x16x128_f8f6f4 v[150:153], v[2:7], v[206:211], v[150:153], v8, v212 op_sel_hi:[0,0,0] cbsz:2 blgp:2
	v_mfma_scale_f32_16x16x128_f8f6f4 v[138:141], v[10:15], v[206:211], v[138:141], v16, v212 op_sel_hi:[0,0,0] cbsz:2 blgp:2
	v_mfma_scale_f32_16x16x128_f8f6f4 v[134:137], v[2:7], v[214:219], v[134:137], v8, v220 op_sel_hi:[0,0,0] cbsz:2 blgp:2
	v_mfma_scale_f32_16x16x128_f8f6f4 v[122:125], v[10:15], v[214:219], v[122:125], v16, v220 op_sel_hi:[0,0,0] cbsz:2 blgp:2
	v_mfma_scale_f32_16x16x128_f8f6f4 v[118:121], v[2:7], v[222:227], v[118:121], v8, v228 op_sel_hi:[0,0,0] cbsz:2 blgp:2
	v_mfma_scale_f32_16x16x128_f8f6f4 v[106:109], v[10:15], v[222:227], v[106:109], v16, v228 op_sel_hi:[0,0,0] cbsz:2 blgp:2
	v_mfma_scale_f32_16x16x128_f8f6f4 v[102:105], v[2:7], v[230:235], v[102:105], v8, v236 op_sel_hi:[0,0,0] cbsz:2 blgp:2
	v_mfma_scale_f32_16x16x128_f8f6f4 v[90:93], v[10:15], v[230:235], v[90:93], v16, v236 op_sel_hi:[0,0,0] cbsz:2 blgp:2
	s_setprio 0
	s_setprio 1
	v_mfma_scale_f32_16x16x128_f8f6f4 v[146:149], v[18:23], v[206:211], v[146:149], v24, v212 op_sel_hi:[0,0,0] cbsz:2 blgp:2
	v_mfma_scale_f32_16x16x128_f8f6f4 v[142:145], v[154:159], v[206:211], v[142:145], v160, v212 op_sel_hi:[0,0,0] cbsz:2 blgp:2
	v_mfma_scale_f32_16x16x128_f8f6f4 v[130:133], v[18:23], v[214:219], v[130:133], v24, v220 op_sel_hi:[0,0,0] cbsz:2 blgp:2
	v_mfma_scale_f32_16x16x128_f8f6f4 v[126:129], v[154:159], v[214:219], v[126:129], v160, v220 op_sel_hi:[0,0,0] cbsz:2 blgp:2
	v_mfma_scale_f32_16x16x128_f8f6f4 v[114:117], v[18:23], v[222:227], v[114:117], v24, v228 op_sel_hi:[0,0,0] cbsz:2 blgp:2
	v_mfma_scale_f32_16x16x128_f8f6f4 v[110:113], v[154:159], v[222:227], v[110:113], v160, v228 op_sel_hi:[0,0,0] cbsz:2 blgp:2
	v_mfma_scale_f32_16x16x128_f8f6f4 v[98:101], v[18:23], v[230:235], v[98:101], v24, v236 op_sel_hi:[0,0,0] cbsz:2 blgp:2
	v_mfma_scale_f32_16x16x128_f8f6f4 v[94:97], v[154:159], v[230:235], v[94:97], v160, v236 op_sel_hi:[0,0,0] cbsz:2 blgp:2
	s_setprio 0
	s_barrier
	s_add_i32 s26, s62, s35
	v_lshl_add_u64 v[164:165], v[184:185], 0, s[6:7]
	s_mov_b32 m0, s26
	ds_read_b128 v[206:209], v198 offset:49152
	ds_read_b128 v[210:213], v198 offset:50176
	ds_read_b128 v[214:217], v198 offset:51200
	ds_read_b128 v[218:221], v198 offset:52224
	ds_read_b128 v[222:225], v198 offset:53248
	ds_read_b128 v[226:229], v198 offset:54272
	ds_read_b128 v[230:233], v198 offset:55296
	ds_read_b128 v[234:237], v198 offset:56320
	global_load_lds_dwordx4 v[164:165], off
	s_add_i32 m0, s26, 0x2000
	s_add_u32 s24, s24, 0x40080
	v_lshl_add_u64 v[164:165], v[186:187], 0, s[6:7]
	s_addc_u32 s25, s25, 0
	s_add_i32 s26, s63, s35
	global_load_lds_dwordx4 v[164:165], off
	s_mov_b32 m0, s26
	s_nop 0
	global_load_lds_dwordx4 v176, s[24:25]
	s_add_i32 m0, s26, 0x2000
	s_nop 0
	global_load_lds_dwordx4 v172, s[24:25]
	v_lshl_add_u64 v[164:165], v[188:189], 0, s[6:7]
	s_mov_b32 m0, s40
	s_nop 0
	global_load_lds_dwordx4 v[164:165], off
	v_lshl_add_u64 v[164:165], v[190:191], 0, s[6:7]
	s_mov_b32 m0, s41
	s_nop 0
	global_load_lds_dwordx4 v[164:165], off
	s_waitcnt vmcnt(8)
	s_waitcnt lgkmcnt(0)
	s_barrier
	s_setprio 1
	s_waitcnt lgkmcnt(0)
	v_mfma_scale_f32_16x16x128_f8f6f4 v[86:89], v[2:7], v[206:211], v[86:89], v8, v212 op_sel_hi:[0,0,0] cbsz:2 blgp:2
	v_mfma_scale_f32_16x16x128_f8f6f4 v[74:77], v[10:15], v[206:211], v[74:77], v16, v212 op_sel_hi:[0,0,0] cbsz:2 blgp:2
	v_mfma_scale_f32_16x16x128_f8f6f4 v[70:73], v[2:7], v[214:219], v[70:73], v8, v220 op_sel_hi:[0,0,0] cbsz:2 blgp:2
	v_mfma_scale_f32_16x16x128_f8f6f4 v[58:61], v[10:15], v[214:219], v[58:61], v16, v220 op_sel_hi:[0,0,0] cbsz:2 blgp:2
	v_mfma_scale_f32_16x16x128_f8f6f4 v[54:57], v[2:7], v[222:227], v[54:57], v8, v228 op_sel_hi:[0,0,0] cbsz:2 blgp:2
	v_mfma_scale_f32_16x16x128_f8f6f4 v[42:45], v[10:15], v[222:227], v[42:45], v16, v228 op_sel_hi:[0,0,0] cbsz:2 blgp:2
	v_mfma_scale_f32_16x16x128_f8f6f4 v[38:41], v[2:7], v[230:235], v[38:41], v8, v236 op_sel_hi:[0,0,0] cbsz:2 blgp:2
	v_mfma_scale_f32_16x16x128_f8f6f4 v[26:29], v[10:15], v[230:235], v[26:29], v16, v236 op_sel_hi:[0,0,0] cbsz:2 blgp:2
	s_setprio 0
	s_setprio 1
	v_mfma_scale_f32_16x16x128_f8f6f4 v[82:85], v[18:23], v[206:211], v[82:85], v24, v212 op_sel_hi:[0,0,0] cbsz:2 blgp:2
	v_mfma_scale_f32_16x16x128_f8f6f4 v[78:81], v[154:159], v[206:211], v[78:81], v160, v212 op_sel_hi:[0,0,0] cbsz:2 blgp:2
	v_mfma_scale_f32_16x16x128_f8f6f4 v[66:69], v[18:23], v[214:219], v[66:69], v24, v220 op_sel_hi:[0,0,0] cbsz:2 blgp:2
	v_mfma_scale_f32_16x16x128_f8f6f4 v[62:65], v[154:159], v[214:219], v[62:65], v160, v220 op_sel_hi:[0,0,0] cbsz:2 blgp:2
	v_mfma_scale_f32_16x16x128_f8f6f4 v[50:53], v[18:23], v[222:227], v[50:53], v24, v228 op_sel_hi:[0,0,0] cbsz:2 blgp:2
	v_mfma_scale_f32_16x16x128_f8f6f4 v[46:49], v[154:159], v[222:227], v[46:49], v160, v228 op_sel_hi:[0,0,0] cbsz:2 blgp:2
	v_mfma_scale_f32_16x16x128_f8f6f4 v[34:37], v[18:23], v[230:235], v[34:37], v24, v236 op_sel_hi:[0,0,0] cbsz:2 blgp:2
	v_mfma_scale_f32_16x16x128_f8f6f4 v[30:33], v[154:159], v[230:235], v[30:33], v160, v236 op_sel_hi:[0,0,0] cbsz:2 blgp:2
	s_setprio 0
	s_barrier
	s_add_i32 s61, s61, 2
	s_add_u32 s22, s22, 0x100
	s_addc_u32 s23, s23, 0
	s_add_u32 s51, s51, 0x100
	s_addc_u32 s60, s60, 0
	s_cmp_gt_u32 s61, 13
	s_cbranch_scc0 .LBB0_1279
	s_and_b64 vcc, exec, s[8:9]
	s_cbranch_vccz .LBB0_1282
	s_barrier
